# P8 Wo epilogue rewritten: 6-deep register pipeline of residual loads + L2 warm-up loads, counted vmcnt, running row pointers
# baseline (speedup 1.0000x reference)
;     __device__ __forceinline__ void operator()(const f32x4 (&acc)[2][2][4][2], const Unit& u, int wr, int wc, int fr, int fq) const {
;         const int row0 = u.pm * BM + wr * 64 + fr, col0 = u.pn * BM + wc * 32 + 8 * fq;
;         f32x4 gv[2][2];
; #pragma unroll
;         for (int bj = 0; bj < 2; ++bj)
; #pragma unroll
;             for (int n = 0; n < 2; ++n) gv[bj][n] = *(const f32x4*)(gate + col0 + bj * HALF + n * 4);
; #pragma unroll
;         for (int ai = 0; ai < 2; ++ai)
; #pragma unroll
;             for (int m = 0; m < 4; ++m) { const size_t off = (size_t)(row0 + ai * HALF + m * 16) * DM + col0;
; #pragma unroll
;                 for (int bj = 0; bj < 2; ++bj) { const f32x4 x0 = *(const f32x4*)(x + off + bj * HALF), x1 = *(const f32x4*)(x + off + bj * HALF + 4);
;                     *(u32x4*)(out + off + bj * HALF) = pack8s(x0 + gv[bj][0] * acc[ai][bj][m][0], x1 + gv[bj][1] * acc[ai][bj][m][1], 1.f); }
;                 if (m & 1) asm volatile("" ::: "memory"); }
;     }
.LBB0_1331:
	v_lshl_add_u32 v160, s74, 8, v165
	v_lshl_or_b32 v158, s75, 8, v167
	v_ashrrev_i32_e32 v161, 31, v160
	v_ashrrev_i32_e32 v159, 31, v158
	v_lshlrev_b64 v[130:131], 11, v[160:161]
	v_lshl_add_u64 v[156:157], v[130:131], 0, v[158:159]
	v_lshl_add_u64 v[134:135], v[158:159], 2, s[24:25]
	s_waitcnt lgkmcnt(0)
	v_lshl_add_u64 v[184:185], v[156:157], 2, s[10:11]
	global_load_dwordx4 v[142:145], v[134:135], off
	global_load_dwordx4 v[138:141], v[134:135], off offset:16
	global_load_dwordx4 v[130:133], v[134:135], off offset:528
	s_nop 0
	global_load_dwordx4 v[134:137], v[134:135], off offset:512
	v_mov_b32_e32 v188, 0x20000
	v_mov_b32_e32 v189, 0
	v_mov_b32_e32 v190, 0x10000
	v_mov_b32_e32 v191, 0
	v_lshl_add_u64 v[186:187], v[156:157], 1, s[38:39]
	v_lshl_add_u64 v[232:233], v[188:189], 0, v[184:185]
	global_load_dwordx4 v[192:195], v[184:185], off
	global_load_dwordx4 v[196:199], v[184:185], off offset:16
	global_load_dwordx4 v[200:203], v[184:185], off offset:512
	global_load_dwordx4 v[204:207], v[184:185], off offset:528
	global_load_dwordx4 v[208:211], v[232:233], off
	global_load_dwordx4 v[212:215], v[232:233], off offset:16
	global_load_dwordx4 v[216:219], v[232:233], off offset:512
	global_load_dwordx4 v[220:223], v[232:233], off offset:528
	v_lshl_add_u64 v[232:233], v[232:233], 0, v[188:189]
	global_load_dwordx4 v[224:227], v[232:233], off
	global_load_dwordx4 v[228:231], v[232:233], off offset:16
	global_load_dwordx4 v[176:179], v[232:233], off offset:512
	global_load_dwordx4 v[180:183], v[232:233], off offset:528
	v_lshl_add_u64 v[232:233], v[232:233], 0, v[188:189]
	global_load_dword v234, v[232:233], off
	global_load_dword v234, v[232:233], off offset:512
	v_lshl_add_u64 v[232:233], v[188:189], 2, v[232:233]
	v_lshl_add_u64 v[232:233], v[232:233], 0, v[188:189]
	global_load_dword v234, v[232:233], off
	global_load_dword v234, v[232:233], off offset:512
	v_lshl_add_u64 v[232:233], v[232:233], 0, v[188:189]
	global_load_dword v234, v[232:233], off
	global_load_dword v234, v[232:233], off offset:512
	v_lshl_add_u64 v[232:233], v[232:233], 0, v[188:189]
	global_load_dword v234, v[232:233], off
	global_load_dword v234, v[232:233], off offset:512
	v_lshl_add_u64 v[232:233], v[232:233], 0, v[188:189]
	global_load_dword v234, v[232:233], off
	global_load_dword v234, v[232:233], off offset:512
	v_lshl_add_u64 v[232:233], v[188:189], 1, v[184:185]
	v_lshl_add_u64 v[232:233], v[188:189], 0, v[232:233]
	s_and_b64 vcc, exec, s[4:5]
	s_mov_b64 s[4:5], -1
	s_waitcnt vmcnt(20)
	v_pk_fma_f32 v[126:127], v[126:127], v[142:143], v[192:193]
	v_pk_fma_f32 v[128:129], v[128:129], v[144:145], v[194:195]
	v_pk_fma_f32 v[122:123], v[122:123], v[138:139], v[196:197]
	v_pk_fma_f32 v[124:125], v[124:125], v[140:141], v[198:199]
	global_load_dwordx4 v[192:195], v[232:233], off
	global_load_dwordx4 v[196:199], v[232:233], off offset:16
	v_cvt_pk_bf16_f32 v126, v126, v127
	v_cvt_pk_bf16_f32 v127, v128, v129
	v_cvt_pk_bf16_f32 v128, v122, v123
	v_cvt_pk_bf16_f32 v129, v124, v125
	global_store_dwordx4 v[186:187], v[126:129], off
	s_waitcnt vmcnt(21)
	v_pk_fma_f32 v[118:119], v[118:119], v[134:135], v[200:201]
	v_pk_fma_f32 v[120:121], v[120:121], v[136:137], v[202:203]
	v_pk_fma_f32 v[114:115], v[114:115], v[130:131], v[204:205]
	v_pk_fma_f32 v[116:117], v[116:117], v[132:133], v[206:207]
	global_load_dwordx4 v[200:203], v[232:233], off offset:512
	global_load_dwordx4 v[204:207], v[232:233], off offset:528
	v_cvt_pk_bf16_f32 v118, v118, v119
	v_cvt_pk_bf16_f32 v119, v120, v121
	v_cvt_pk_bf16_f32 v120, v114, v115
	v_cvt_pk_bf16_f32 v121, v116, v117
	global_store_dwordx4 v[186:187], v[118:121], off offset:256
	v_lshl_add_u64 v[186:187], v[186:187], 0, v[190:191]
	s_waitcnt vmcnt(22)
	v_pk_fma_f32 v[110:111], v[110:111], v[142:143], v[208:209]
	v_pk_fma_f32 v[112:113], v[112:113], v[144:145], v[210:211]
	v_pk_fma_f32 v[106:107], v[106:107], v[138:139], v[212:213]
	v_pk_fma_f32 v[108:109], v[108:109], v[140:141], v[214:215]
	v_lshl_add_u64 v[232:233], v[188:189], 2, v[232:233]
	v_lshl_add_u64 v[232:233], v[232:233], 0, v[188:189]
	global_load_dwordx4 v[208:211], v[232:233], off
	global_load_dwordx4 v[212:215], v[232:233], off offset:16
	v_cvt_pk_bf16_f32 v110, v110, v111
	v_cvt_pk_bf16_f32 v111, v112, v113
	v_cvt_pk_bf16_f32 v112, v106, v107
	v_cvt_pk_bf16_f32 v113, v108, v109
	global_store_dwordx4 v[186:187], v[110:113], off
	s_waitcnt vmcnt(23)
	v_pk_fma_f32 v[102:103], v[102:103], v[134:135], v[216:217]
	v_pk_fma_f32 v[104:105], v[104:105], v[136:137], v[218:219]
	v_pk_fma_f32 v[98:99], v[98:99], v[130:131], v[220:221]
	v_pk_fma_f32 v[100:101], v[100:101], v[132:133], v[222:223]
	global_load_dwordx4 v[216:219], v[232:233], off offset:512
	global_load_dwordx4 v[220:223], v[232:233], off offset:528
	v_cvt_pk_bf16_f32 v102, v102, v103
	v_cvt_pk_bf16_f32 v103, v104, v105
	v_cvt_pk_bf16_f32 v104, v98, v99
	v_cvt_pk_bf16_f32 v105, v100, v101
	global_store_dwordx4 v[186:187], v[102:105], off offset:256
	v_lshl_add_u64 v[186:187], v[186:187], 0, v[190:191]
	s_waitcnt vmcnt(24)
	v_pk_fma_f32 v[94:95], v[94:95], v[142:143], v[224:225]
	v_pk_fma_f32 v[96:97], v[96:97], v[144:145], v[226:227]
	v_pk_fma_f32 v[90:91], v[90:91], v[138:139], v[228:229]
	v_pk_fma_f32 v[92:93], v[92:93], v[140:141], v[230:231]
	v_lshl_add_u64 v[232:233], v[232:233], 0, v[188:189]
	global_load_dwordx4 v[224:227], v[232:233], off
	global_load_dwordx4 v[228:231], v[232:233], off offset:16
	v_cvt_pk_bf16_f32 v94, v94, v95
	v_cvt_pk_bf16_f32 v95, v96, v97
	v_cvt_pk_bf16_f32 v96, v90, v91
	v_cvt_pk_bf16_f32 v97, v92, v93
	global_store_dwordx4 v[186:187], v[94:97], off
	s_waitcnt vmcnt(25)
;     __device__ __forceinline__ void operator()(const f32x4 (&acc)[2][2][4][2], const Unit& u, int wr, int wc, int fr, int fq) const {
;     ...
;         for (int ai = 0; ai < 2; ++ai)
; #pragma unroll
;             for (int m = 0; m < 4; ++m) { const size_t off = (size_t)(row0 + ai * HALF + m * 16) * DM + col0;
; #pragma unroll
;                 for (int bj = 0; bj < 2; ++bj) { const f32x4 x0 = *(const f32x4*)(x + off + bj * HALF), x1 = *(const f32x4*)(x + off + bj * HALF + 4);
;                     *(u32x4*)(out + off + bj * HALF) = pack8s(x0 + gv[bj][0] * acc[ai][bj][m][0], x1 + gv[bj][1] * acc[ai][bj][m][1], 1.f); }
;                 if (m & 1) asm volatile("" ::: "memory"); }
	v_pk_fma_f32 v[86:87], v[86:87], v[134:135], v[176:177]
	v_pk_fma_f32 v[88:89], v[88:89], v[136:137], v[178:179]
	v_pk_fma_f32 v[82:83], v[82:83], v[130:131], v[180:181]
	v_pk_fma_f32 v[84:85], v[84:85], v[132:133], v[182:183]
	global_load_dwordx4 v[176:179], v[232:233], off offset:512
	global_load_dwordx4 v[180:183], v[232:233], off offset:528
	v_cvt_pk_bf16_f32 v86, v86, v87
	v_cvt_pk_bf16_f32 v87, v88, v89
	v_cvt_pk_bf16_f32 v88, v82, v83
	v_cvt_pk_bf16_f32 v89, v84, v85
	global_store_dwordx4 v[186:187], v[86:89], off offset:256
	v_lshl_add_u64 v[186:187], v[186:187], 0, v[190:191]
	s_waitcnt vmcnt(16)
	v_pk_fma_f32 v[78:79], v[78:79], v[142:143], v[192:193]
	v_pk_fma_f32 v[80:81], v[80:81], v[144:145], v[194:195]
	v_pk_fma_f32 v[74:75], v[74:75], v[138:139], v[196:197]
	v_pk_fma_f32 v[76:77], v[76:77], v[140:141], v[198:199]
	v_lshl_add_u64 v[232:233], v[232:233], 0, v[188:189]
	global_load_dwordx4 v[192:195], v[232:233], off
	global_load_dwordx4 v[196:199], v[232:233], off offset:16
	v_cvt_pk_bf16_f32 v78, v78, v79
	v_cvt_pk_bf16_f32 v79, v80, v81
	v_cvt_pk_bf16_f32 v80, v74, v75
	v_cvt_pk_bf16_f32 v81, v76, v77
	global_store_dwordx4 v[186:187], v[78:81], off
	s_waitcnt vmcnt(16)
	v_pk_fma_f32 v[70:71], v[70:71], v[134:135], v[200:201]
	v_pk_fma_f32 v[72:73], v[72:73], v[136:137], v[202:203]
	v_pk_fma_f32 v[66:67], v[66:67], v[130:131], v[204:205]
	v_pk_fma_f32 v[68:69], v[68:69], v[132:133], v[206:207]
	global_load_dwordx4 v[200:203], v[232:233], off offset:512
	global_load_dwordx4 v[204:207], v[232:233], off offset:528
	v_cvt_pk_bf16_f32 v70, v70, v71
	v_cvt_pk_bf16_f32 v71, v72, v73
	v_cvt_pk_bf16_f32 v72, v66, v67
	v_cvt_pk_bf16_f32 v73, v68, v69
	global_store_dwordx4 v[186:187], v[70:73], off offset:256
	v_lshl_add_u64 v[186:187], v[190:191], 2, v[186:187]
	v_lshl_add_u64 v[186:187], v[186:187], 0, v[190:191]
	s_waitcnt vmcnt(16)
	v_pk_fma_f32 v[62:63], v[62:63], v[142:143], v[208:209]
	v_pk_fma_f32 v[64:65], v[64:65], v[144:145], v[210:211]
	v_pk_fma_f32 v[58:59], v[58:59], v[138:139], v[212:213]
	v_pk_fma_f32 v[60:61], v[60:61], v[140:141], v[214:215]
	v_lshl_add_u64 v[232:233], v[232:233], 0, v[188:189]
	global_load_dwordx4 v[208:211], v[232:233], off
	global_load_dwordx4 v[212:215], v[232:233], off offset:16
	v_cvt_pk_bf16_f32 v62, v62, v63
	v_cvt_pk_bf16_f32 v63, v64, v65
	v_cvt_pk_bf16_f32 v64, v58, v59
	v_cvt_pk_bf16_f32 v65, v60, v61
	global_store_dwordx4 v[186:187], v[62:65], off
	s_waitcnt vmcnt(16)
	v_pk_fma_f32 v[54:55], v[54:55], v[134:135], v[216:217]
	v_pk_fma_f32 v[56:57], v[56:57], v[136:137], v[218:219]
	v_pk_fma_f32 v[50:51], v[50:51], v[130:131], v[220:221]
	v_pk_fma_f32 v[52:53], v[52:53], v[132:133], v[222:223]
	global_load_dwordx4 v[216:219], v[232:233], off offset:512
	global_load_dwordx4 v[220:223], v[232:233], off offset:528
	v_cvt_pk_bf16_f32 v54, v54, v55
	v_cvt_pk_bf16_f32 v55, v56, v57
	v_cvt_pk_bf16_f32 v56, v50, v51
	v_cvt_pk_bf16_f32 v57, v52, v53
	global_store_dwordx4 v[186:187], v[54:57], off offset:256
	v_lshl_add_u64 v[186:187], v[186:187], 0, v[190:191]
	s_waitcnt vmcnt(16)
	v_pk_fma_f32 v[46:47], v[46:47], v[142:143], v[224:225]
	v_pk_fma_f32 v[48:49], v[48:49], v[144:145], v[226:227]
	v_pk_fma_f32 v[42:43], v[42:43], v[138:139], v[228:229]
	v_pk_fma_f32 v[44:45], v[44:45], v[140:141], v[230:231]
	v_cvt_pk_bf16_f32 v46, v46, v47
	v_cvt_pk_bf16_f32 v47, v48, v49
	v_cvt_pk_bf16_f32 v48, v42, v43
	v_cvt_pk_bf16_f32 v49, v44, v45
	global_store_dwordx4 v[186:187], v[46:49], off
	s_waitcnt vmcnt(14)
	v_pk_fma_f32 v[38:39], v[38:39], v[134:135], v[176:177]
	v_pk_fma_f32 v[40:41], v[40:41], v[136:137], v[178:179]
	v_pk_fma_f32 v[34:35], v[34:35], v[130:131], v[180:181]
	v_pk_fma_f32 v[36:37], v[36:37], v[132:133], v[182:183]
	v_cvt_pk_bf16_f32 v38, v38, v39
	v_cvt_pk_bf16_f32 v39, v40, v41
	v_cvt_pk_bf16_f32 v40, v34, v35
	v_cvt_pk_bf16_f32 v41, v36, v37
	global_store_dwordx4 v[186:187], v[38:41], off offset:256
	v_lshl_add_u64 v[186:187], v[186:187], 0, v[190:191]
	s_waitcnt vmcnt(12)
	v_pk_fma_f32 v[30:31], v[30:31], v[142:143], v[192:193]
	v_pk_fma_f32 v[32:33], v[32:33], v[144:145], v[194:195]
	v_pk_fma_f32 v[26:27], v[26:27], v[138:139], v[196:197]
	v_pk_fma_f32 v[28:29], v[28:29], v[140:141], v[198:199]
	v_cvt_pk_bf16_f32 v30, v30, v31
	v_cvt_pk_bf16_f32 v31, v32, v33
	v_cvt_pk_bf16_f32 v32, v26, v27
	v_cvt_pk_bf16_f32 v33, v28, v29
	global_store_dwordx4 v[186:187], v[30:33], off
	s_waitcnt vmcnt(10)
	v_pk_fma_f32 v[22:23], v[22:23], v[134:135], v[200:201]
	v_pk_fma_f32 v[24:25], v[24:25], v[136:137], v[202:203]
	v_pk_fma_f32 v[18:19], v[18:19], v[130:131], v[204:205]
	v_pk_fma_f32 v[20:21], v[20:21], v[132:133], v[206:207]
	v_cvt_pk_bf16_f32 v22, v22, v23
	v_cvt_pk_bf16_f32 v23, v24, v25
	v_cvt_pk_bf16_f32 v24, v18, v19
	v_cvt_pk_bf16_f32 v25, v20, v21
	global_store_dwordx4 v[186:187], v[22:25], off offset:256
	v_lshl_add_u64 v[186:187], v[186:187], 0, v[190:191]
	s_waitcnt vmcnt(8)
	v_pk_fma_f32 v[14:15], v[14:15], v[142:143], v[208:209]
	v_pk_fma_f32 v[16:17], v[16:17], v[144:145], v[210:211]
	v_pk_fma_f32 v[10:11], v[10:11], v[138:139], v[212:213]
	v_pk_fma_f32 v[12:13], v[12:13], v[140:141], v[214:215]
	v_cvt_pk_bf16_f32 v14, v14, v15
	v_cvt_pk_bf16_f32 v15, v16, v17
	v_cvt_pk_bf16_f32 v16, v10, v11
	v_cvt_pk_bf16_f32 v17, v12, v13
	global_store_dwordx4 v[186:187], v[14:17], off
	s_waitcnt vmcnt(6)
	v_pk_fma_f32 v[6:7], v[6:7], v[134:135], v[216:217]
	v_pk_fma_f32 v[8:9], v[8:9], v[136:137], v[218:219]
	v_pk_fma_f32 v[2:3], v[2:3], v[130:131], v[220:221]
	v_pk_fma_f32 v[4:5], v[4:5], v[132:133], v[222:223]
	v_cvt_pk_bf16_f32 v6, v6, v7
	v_cvt_pk_bf16_f32 v7, v8, v9
	v_cvt_pk_bf16_f32 v8, v2, v3
	v_cvt_pk_bf16_f32 v9, v4, v5
	global_store_dwordx4 v[186:187], v[6:9], off offset:256
	s_cbranch_vccnz .LBB0_1315
	s_andn2_b64 vcc, exec, s[22:23]
	s_cbranch_vccnz .LBB0_1314
	s_barrier
	s_branch .LBB0_1314
